# GQA loop: part of the next tile's exps moved into the under-full PV gaps
# baseline (speedup 1.0000x reference)
; #define LAS __attribute__((address_space(3)))
; __device__ __forceinline__ void finishSM(f32x16& p0, f32x16& p1, float alpha, float& l_reg, bf16x8& pa0, bf16x8& pa1, bf16x8& pa2, bf16x8& pa3) {
; #pragma unroll
;     for (int r = 0; r < 16; ++r) p1[r] = EXP_PROBE ? fmaf(p1[r], 0.001f, 1.f) : __builtin_amdgcn_exp2f(p1[r]);
;     float ps = 0.f;
; #pragma unroll
;     for (int r = 0; r < 16; ++r) ps += p0[r];
; #pragma unroll
;     for (int r = 0; r < 16; ++r) ps += p1[r];
;     { auto rr = __builtin_amdgcn_permlane32_swap(__float_as_uint(ps), __float_as_uint(ps), false, false);
;       ps = __uint_as_float(rr[0]) + __uint_as_float(rr[1]); }
;     l_reg = l_reg * alpha + ps;
;     ATT_PKN(p0, 0, pa0); ATT_PKN(p0, 8, pa1); ATT_PKN(p1, 0, pa2); ATT_PKN(p1, 8, pa3);
; }
; template <int DQK> __device__ __forceinline__ void qkt(f32x16& p0, f32x16& p1, const LAS char* buf, const bf16x8* qr, int r32, int hi, const f32x16& negm) {
; #pragma unroll
;     for (int d0 = 0; d0 < 4; ++d0) { const int ch = d0 * 2 + hi;
;         const bf16x8 b0 = *(const LAS bf16x8*)(buf + B_KN + swz64(r32, ch));
;         const bf16x8 b1 = *(const LAS bf16x8*)(buf + B_KN + swz64(32 + r32, ch));
;         p0 = __builtin_amdgcn_mfma_f32_32x32x16_bf16(b0, qr[d0], d0 == 0 ? negm : p0, 0, 0, 0);
;         p1 = __builtin_amdgcn_mfma_f32_32x32x16_bf16(b1, qr[d0], d0 == 0 ? negm : p1, 0, 0, 0); }
; template <bool FIXM> __device__ __forceinline__ void pv_psm(f32x16& o0, f32x16& o1, unsigned vb, bf16x8 pa0, bf16x8 pa1, bf16x8 pa2, bf16x8 pa3,
;                                        f32x16& p0, f32x16& p1, float& m_reg, f32x16& negm, float& alpha) {
;     { const s16x4 l0 = tr_read<v_rd_off(0, 0, 0)>(vb), h0 = tr_read<v_rd_off(0, 0, 1)>(vb), l1 = tr_read<v_rd_off(0, 1, 0)>(vb), h1 = tr_read<v_rd_off(0, 1, 1)>(vb);
;       const s16x4 l2 = tr_read<v_rd_off(0, 2, 0)>(vb), h2 = tr_read<v_rd_off(0, 2, 1)>(vb), l3 = tr_read<v_rd_off(0, 3, 0)>(vb), h3 = tr_read<v_rd_off(0, 3, 1)>(vb);
;       float pmax = 0.f; SBAR(); if (!FIXM) pmax = psm_max(p0, p1); else { _Pragma("unroll") for (int r = 0; r < 8; ++r) p0[r] = __builtin_amdgcn_exp2f(p0[r]); } SBAR();
;       asm volatile("s_waitcnt lgkmcnt(0)" ::: "memory"); SBAR();
;       o0 = __builtin_amdgcn_mfma_f32_32x32x16_bf16(ATT_PK(l0, h0), pa0, o0, 0, 0, 0);
;       o0 = __builtin_amdgcn_mfma_f32_32x32x16_bf16(ATT_PK(l1, h1), pa1, o0, 0, 0, 0);
.LBB0_497:
	s_mov_b32 s1, s11
	s_mov_b32 s11, s35
	s_waitcnt lgkmcnt(0)
	s_barrier
	v_add_u32_e32 v252, s1, v208
	v_add_u32_e32 v228, v252, v209
	ds_read_b128 v[224:227], v228
	ds_read_b128 v[228:231], v228 offset:4096
	v_add_u32_e32 v236, v252, v210
	ds_read_b128 v[232:235], v236
	ds_read_b128 v[236:239], v236 offset:4096
	v_add_u32_e32 v244, v252, v211
	ds_read_b128 v[240:243], v244
	ds_read_b128 v[244:247], v244 offset:4096
	v_add_u32_e32 v253, v252, v212
	ds_read_b128 v[248:251], v253
	v_exp_f32_e32 v66, v66
	v_exp_f32_e32 v67, v67
	v_exp_f32_e32 v68, v68
	v_exp_f32_e32 v69, v69
	v_exp_f32_e32 v70, v70
	v_exp_f32_e32 v71, v71
	v_exp_f32_e32 v72, v72
	v_exp_f32_e32 v73, v73
	s_waitcnt lgkmcnt(6)
	v_mfma_f32_32x32x16_bf16 v[98:113], v[224:227], v[114:117], v[18:33]
	ds_read_b128 v[224:227], v253 offset:4096
	v_exp_f32_e32 v74, v74
	v_exp_f32_e32 v75, v75
	v_exp_f32_e32 v76, v76
	v_cvt_pk_bf16_f32 v156, v143, v145
	v_cvt_pk_bf16_f32 v157, v141, v144
	v_add_f32_e32 v164, 0, v143
	v_add_f32_e32 v164, v145, v164
	v_add_f32_e32 v164, v141, v164
	s_waitcnt lgkmcnt(6)
	v_mfma_f32_32x32x16_bf16 v[82:97], v[228:231], v[114:117], v[18:33]
	v_exp_f32_e32 v77, v77
	v_exp_f32_e32 v78, v78
	v_exp_f32_e32 v79, v79
	v_cvt_pk_bf16_f32 v158, v139, v142
	v_cvt_pk_bf16_f32 v159, v138, v140
	v_add_f32_e32 v164, v144, v164
	v_add_f32_e32 v164, v139, v164
	v_add_f32_e32 v164, v142, v164
	s_waitcnt lgkmcnt(5)
	v_mfma_f32_32x32x16_bf16 v[98:113], v[232:235], v[12:15], v[98:113]
	v_exp_f32_e32 v80, v80
	v_exp_f32_e32 v81, v81
	v_cvt_pk_bf16_f32 v160, v151, v153
	v_cvt_pk_bf16_f32 v161, v149, v152
	v_cvt_pk_bf16_f32 v162, v147, v150
	v_cvt_pk_bf16_f32 v163, v146, v148
	v_add_f32_e32 v164, v138, v164
	v_add_f32_e32 v164, v140, v164
	v_add_f32_e32 v164, v151, v164
	s_waitcnt lgkmcnt(4)
	v_mfma_f32_32x32x16_bf16 v[82:97], v[236:239], v[12:15], v[82:97]
	v_add_f32_e32 v164, v153, v164
	v_add_f32_e32 v164, v149, v164
	v_add_f32_e32 v164, v152, v164
	v_add_f32_e32 v164, v147, v164
	v_add_f32_e32 v164, v150, v164
	v_add_f32_e32 v164, v146, v164
	v_add_f32_e32 v164, v148, v164
	s_waitcnt lgkmcnt(3)
	v_mfma_f32_32x32x16_bf16 v[98:113], v[240:243], v[8:11], v[98:113]
	v_add_u32_e32 v2, s11, v213
	ds_read_b64_tr_b16 v[138:139], v2 offset:0
	ds_read_b64_tr_b16 v[140:141], v2 offset:1024
	ds_read_b64_tr_b16 v[142:143], v2 offset:2048
	ds_read_b64_tr_b16 v[144:145], v2 offset:3072
	v_add_f32_e32 v164, v66, v164
	v_add_f32_e32 v164, v67, v164
	v_add_f32_e32 v164, v68, v164
	v_add_f32_e32 v164, v69, v164
	s_waitcnt lgkmcnt(6)
	v_mfma_f32_32x32x16_bf16 v[82:97], v[244:247], v[8:11], v[82:97]
	ds_read_b64_tr_b16 v[146:147], v2 offset:4096
	ds_read_b64_tr_b16 v[148:149], v2 offset:5120
	ds_read_b64_tr_b16 v[150:151], v2 offset:6144
	ds_read_b64_tr_b16 v[152:153], v2 offset:7168
	v_add_f32_e32 v164, v70, v164
	v_add_f32_e32 v164, v71, v164
	v_add_f32_e32 v164, v72, v164
	v_add_f32_e32 v164, v73, v164
	s_waitcnt lgkmcnt(9)
	v_mfma_f32_32x32x16_bf16 v[98:113], v[248:251], v[4:7], v[98:113]
	v_add_f32_e32 v164, v74, v164
	v_add_f32_e32 v164, v75, v164
	v_add_f32_e32 v164, v76, v164
	v_add_f32_e32 v164, v77, v164
	s_waitcnt lgkmcnt(8)
	v_mfma_f32_32x32x16_bf16 v[82:97], v[224:227], v[4:7], v[82:97]
	ds_read_b64_tr_b16 v[224:225], v2 offset:512
	ds_read_b64_tr_b16 v[226:227], v2 offset:1536
	ds_read_b64_tr_b16 v[228:229], v2 offset:2560
	ds_read_b64_tr_b16 v[230:231], v2 offset:3584
	ds_read_b64_tr_b16 v[232:233], v2 offset:4608
	ds_read_b64_tr_b16 v[234:235], v2 offset:5632
	ds_read_b64_tr_b16 v[236:237], v2 offset:6656
	ds_read_b64_tr_b16 v[238:239], v2 offset:7680
	v_exp_f32_e32 v168, v98
	v_exp_f32_e32 v169, v99
	v_exp_f32_e32 v170, v100
	s_waitcnt lgkmcnt(8)
	v_mfma_f32_32x32x16_bf16 v[50:65], v[138:141], v[156:159], v[50:65]
	v_add_f32_e32 v164, v78, v164
	v_add_f32_e32 v164, v79, v164
	v_add_f32_e32 v164, v80, v164
	v_add_f32_e32 v154, v81, v164
	v_mov_b32_e32 v155, v154
	v_mfma_f32_32x32x16_bf16 v[50:65], v[142:145], v[160:163], v[50:65]
	v_cvt_pk_bf16_f32 v66, v66, v67
	v_cvt_pk_bf16_f32 v67, v68, v69
	v_cvt_pk_bf16_f32 v68, v70, v71
	v_cvt_pk_bf16_f32 v69, v72, v73
	v_cvt_pk_bf16_f32 v70, v74, v75
	v_cvt_pk_bf16_f32 v71, v76, v77
	v_cvt_pk_bf16_f32 v72, v78, v79
	v_cvt_pk_bf16_f32 v73, v80, v81
	v_permlane32_swap_b32_e32 v154, v155
	v_mfma_f32_32x32x16_bf16 v[50:65], v[146:149], v[66:69], v[50:65]
	s_add_i32 s8, s13, -1
	s_cmp_lt_u32 s8, s31
	s_cselect_b32 s9, 0, s31
	s_cselect_b32 s35, s12, s29
	s_lshl_b32 s9, s9, 6
	s_sub_i32 s9, s35, s9
	v_add_u32_e32 v252, s9, v137
	v_subrev_u32_e32 v126, 64, v252
	v_ashrrev_i32_e32 v127, 31, v126
	v_exp_f32_e32 v171, v101
	v_mfma_f32_32x32x16_bf16 v[50:65], v[150:153], v[70:73], v[50:65]
	v_lshlrev_b64 v[126:127], 8, v[126:127]
	v_lshl_add_u64 v[128:129], v[16:17], 0, v[126:127]
	v_lshl_add_u64 v[126:127], v[134:135], 0, v[126:127]
	global_load_dwordx4 v[130:133], v[128:129], off
	s_nop 0
	global_load_dwordx4 v[126:129], v[126:127], off
	s_waitcnt lgkmcnt(0)
	v_mfma_f32_32x32x16_bf16 v[34:49], v[224:227], v[156:159], v[34:49]
	s_waitcnt vmcnt(2)
	v_add_u32_e32 v165, s10, v187
	ds_write_b128 v165, v[118:121]
	v_add_u32_e32 v165, s10, v214
	ds_write_b128 v165, v[122:125] offset:12288
	v_exp_f32_e32 v172, v102
	v_exp_f32_e32 v173, v103
	v_mfma_f32_32x32x16_bf16 v[34:49], v[228:231], v[160:163], v[34:49]
	v_exp_f32_e32 v174, v104
	v_exp_f32_e32 v175, v105
	v_exp_f32_e32 v176, v106
	v_mfma_f32_32x32x16_bf16 v[34:49], v[232:235], v[66:69], v[34:49]
	v_exp_f32_e32 v177, v107
	v_exp_f32_e32 v178, v108
	v_exp_f32_e32 v179, v109
	v_mfma_f32_32x32x16_bf16 v[34:49], v[236:239], v[70:73], v[34:49]
	v_exp_f32_e32 v180, v110
	v_exp_f32_e32 v181, v111
	v_exp_f32_e32 v182, v112
	v_exp_f32_e32 v183, v113
	s_waitcnt lgkmcnt(0)
	s_barrier
; #define LAS __attribute__((address_space(3)))
; __device__ __forceinline__ void finishSM(f32x16& p0, f32x16& p1, float alpha, float& l_reg, bf16x8& pa0, bf16x8& pa1, bf16x8& pa2, bf16x8& pa3) {
; #pragma unroll
;     for (int r = 0; r < 16; ++r) p1[r] = EXP_PROBE ? fmaf(p1[r], 0.001f, 1.f) : __builtin_amdgcn_exp2f(p1[r]);
;     float ps = 0.f;
; #pragma unroll
;     for (int r = 0; r < 16; ++r) ps += p0[r];
; #pragma unroll
;     for (int r = 0; r < 16; ++r) ps += p1[r];
;     { auto rr = __builtin_amdgcn_permlane32_swap(__float_as_uint(ps), __float_as_uint(ps), false, false);
;       ps = __uint_as_float(rr[0]) + __uint_as_float(rr[1]); }
;     l_reg = l_reg * alpha + ps;
;     ATT_PKN(p0, 0, pa0); ATT_PKN(p0, 8, pa1); ATT_PKN(p1, 0, pa2); ATT_PKN(p1, 8, pa3);
; }
; template <int DQK> __device__ __forceinline__ void qkt(f32x16& p0, f32x16& p1, const LAS char* buf, const bf16x8* qr, int r32, int hi, const f32x16& negm) {
; #pragma unroll
;     for (int d0 = 0; d0 < 4; ++d0) { const int ch = d0 * 2 + hi;
;         const bf16x8 b0 = *(const LAS bf16x8*)(buf + B_KN + swz64(r32, ch));
;         const bf16x8 b1 = *(const LAS bf16x8*)(buf + B_KN + swz64(32 + r32, ch));
;         p0 = __builtin_amdgcn_mfma_f32_32x32x16_bf16(b0, qr[d0], d0 == 0 ? negm : p0, 0, 0, 0);
;         p1 = __builtin_amdgcn_mfma_f32_32x32x16_bf16(b1, qr[d0], d0 == 0 ? negm : p1, 0, 0, 0); }
; template <bool FIXM> __device__ __forceinline__ void pv_psm(f32x16& o0, f32x16& o1, unsigned vb, bf16x8 pa0, bf16x8 pa1, bf16x8 pa2, bf16x8 pa3,
;                                        f32x16& p0, f32x16& p1, float& m_reg, f32x16& negm, float& alpha) {
;     { const s16x4 l0 = tr_read<v_rd_off(0, 0, 0)>(vb), h0 = tr_read<v_rd_off(0, 0, 1)>(vb), l1 = tr_read<v_rd_off(0, 1, 0)>(vb), h1 = tr_read<v_rd_off(0, 1, 1)>(vb);
;       const s16x4 l2 = tr_read<v_rd_off(0, 2, 0)>(vb), h2 = tr_read<v_rd_off(0, 2, 1)>(vb), l3 = tr_read<v_rd_off(0, 3, 0)>(vb), h3 = tr_read<v_rd_off(0, 3, 1)>(vb);
;       float pmax = 0.f; SBAR(); if (!FIXM) pmax = psm_max(p0, p1); else { _Pragma("unroll") for (int r = 0; r < 8; ++r) p0[r] = __builtin_amdgcn_exp2f(p0[r]); } SBAR();
;       asm volatile("s_waitcnt lgkmcnt(0)" ::: "memory"); SBAR();
;       o0 = __builtin_amdgcn_mfma_f32_32x32x16_bf16(ATT_PK(l0, h0), pa0, o0, 0, 0, 0);
;       o0 = __builtin_amdgcn_mfma_f32_32x32x16_bf16(ATT_PK(l1, h1), pa1, o0, 0, 0, 0);
	v_add_u32_e32 v252, s10, v201
	v_add_u32_e32 v228, v252, v209
	ds_read_b128 v[224:227], v228
	ds_read_b128 v[228:231], v228 offset:4096
	v_add_u32_e32 v236, v252, v210
	ds_read_b128 v[232:235], v236
	ds_read_b128 v[236:239], v236 offset:4096
	v_add_u32_e32 v244, v252, v211
	ds_read_b128 v[240:243], v244
	ds_read_b128 v[244:247], v244 offset:4096
	v_add_u32_e32 v253, v252, v212
	ds_read_b128 v[248:251], v253
	v_exp_f32_e32 v82, v82
	v_exp_f32_e32 v83, v83
	v_exp_f32_e32 v84, v84
	v_exp_f32_e32 v85, v85
	v_exp_f32_e32 v86, v86
	v_exp_f32_e32 v87, v87
	v_exp_f32_e32 v88, v88
	v_exp_f32_e32 v89, v89
	s_waitcnt lgkmcnt(6)
	v_mfma_f32_32x32x16_bf16 v[98:113], v[224:227], v[114:117], v[18:33]
	ds_read_b128 v[224:227], v253 offset:4096
	v_exp_f32_e32 v90, v90
	v_exp_f32_e32 v91, v91
	v_exp_f32_e32 v92, v92
	v_cvt_pk_bf16_f32 v156, v168, v169
	v_cvt_pk_bf16_f32 v157, v170, v171
	v_add_f32_e32 v164, 0, v168
	v_add_f32_e32 v164, v169, v164
	v_add_f32_e32 v164, v170, v164
	s_waitcnt lgkmcnt(6)
	v_mfma_f32_32x32x16_bf16 v[66:81], v[228:231], v[114:117], v[18:33]
	v_exp_f32_e32 v93, v93
	v_exp_f32_e32 v94, v94
	v_exp_f32_e32 v95, v95
	v_cvt_pk_bf16_f32 v158, v172, v173
	v_cvt_pk_bf16_f32 v159, v174, v175
	v_add_f32_e32 v164, v171, v164
	v_add_f32_e32 v164, v172, v164
	v_add_f32_e32 v164, v173, v164
	s_waitcnt lgkmcnt(5)
	v_mfma_f32_32x32x16_bf16 v[98:113], v[232:235], v[12:15], v[98:113]
	v_exp_f32_e32 v96, v96
	v_exp_f32_e32 v97, v97
	v_cvt_pk_bf16_f32 v160, v176, v177
	v_cvt_pk_bf16_f32 v161, v178, v179
	v_cvt_pk_bf16_f32 v162, v180, v181
	v_cvt_pk_bf16_f32 v163, v182, v183
	v_add_f32_e32 v164, v174, v164
	v_add_f32_e32 v164, v175, v164
	v_add_f32_e32 v164, v176, v164
	s_waitcnt lgkmcnt(4)
	v_mfma_f32_32x32x16_bf16 v[66:81], v[236:239], v[12:15], v[66:81]
	v_add_f32_e32 v164, v177, v164
	v_add_f32_e32 v164, v178, v164
	v_add_f32_e32 v164, v179, v164
	v_add_f32_e32 v164, v180, v164
	v_add_f32_e32 v164, v181, v164
	v_add_f32_e32 v164, v182, v164
	v_add_f32_e32 v164, v183, v164
	s_waitcnt lgkmcnt(3)
	v_mfma_f32_32x32x16_bf16 v[98:113], v[240:243], v[8:11], v[98:113]
	v_add_u32_e32 v253, s1, v213
	ds_read_b64_tr_b16 v[168:169], v253 offset:0
	ds_read_b64_tr_b16 v[170:171], v253 offset:1024
	ds_read_b64_tr_b16 v[172:173], v253 offset:2048
	ds_read_b64_tr_b16 v[174:175], v253 offset:3072
	v_add_f32_e32 v164, v82, v164
	v_add_f32_e32 v164, v83, v164
	v_add_f32_e32 v164, v84, v164
	v_add_f32_e32 v164, v85, v164
	s_waitcnt lgkmcnt(6)
	v_mfma_f32_32x32x16_bf16 v[66:81], v[244:247], v[8:11], v[66:81]
	ds_read_b64_tr_b16 v[176:177], v253 offset:4096
	ds_read_b64_tr_b16 v[178:179], v253 offset:5120
	ds_read_b64_tr_b16 v[180:181], v253 offset:6144
	ds_read_b64_tr_b16 v[182:183], v253 offset:7168
	v_add_f32_e32 v164, v86, v164
	v_add_f32_e32 v164, v87, v164
	v_add_f32_e32 v164, v88, v164
	v_add_f32_e32 v164, v89, v164
	s_waitcnt lgkmcnt(9)
	v_mfma_f32_32x32x16_bf16 v[98:113], v[248:251], v[4:7], v[98:113]
	v_add_f32_e32 v164, v90, v164
	v_add_f32_e32 v164, v91, v164
	v_add_f32_e32 v164, v92, v164
	v_add_f32_e32 v164, v93, v164
	s_waitcnt lgkmcnt(8)
	v_mfma_f32_32x32x16_bf16 v[66:81], v[224:227], v[4:7], v[66:81]
	ds_read_b64_tr_b16 v[224:225], v253 offset:512
	ds_read_b64_tr_b16 v[226:227], v253 offset:1536
	ds_read_b64_tr_b16 v[228:229], v253 offset:2560
	ds_read_b64_tr_b16 v[230:231], v253 offset:3584
	ds_read_b64_tr_b16 v[232:233], v253 offset:4608
	ds_read_b64_tr_b16 v[234:235], v253 offset:5632
	ds_read_b64_tr_b16 v[236:237], v253 offset:6656
	ds_read_b64_tr_b16 v[238:239], v253 offset:7680
	v_exp_f32_e32 v143, v98
	v_exp_f32_e32 v145, v99
	v_exp_f32_e32 v141, v100
	s_waitcnt lgkmcnt(8)
	v_mfma_f32_32x32x16_bf16 v[50:65], v[168:171], v[156:159], v[50:65]
	v_add_f32_e32 v164, v94, v164
	v_add_f32_e32 v164, v95, v164
	v_add_f32_e32 v164, v96, v164
	v_add_f32_e32 v164, v97, v164
	v_mov_b32_e32 v165, v164
	v_mfma_f32_32x32x16_bf16 v[50:65], v[172:175], v[160:163], v[50:65]
	v_cvt_pk_bf16_f32 v82, v82, v83
	v_cvt_pk_bf16_f32 v83, v84, v85
	v_cvt_pk_bf16_f32 v84, v86, v87
	v_cvt_pk_bf16_f32 v85, v88, v89
	v_cvt_pk_bf16_f32 v86, v90, v91
	v_cvt_pk_bf16_f32 v87, v92, v93
	v_cvt_pk_bf16_f32 v88, v94, v95
	v_cvt_pk_bf16_f32 v89, v96, v97
	v_permlane32_swap_b32_e32 v164, v165
	v_mfma_f32_32x32x16_bf16 v[50:65], v[176:179], v[82:85], v[50:65]
	v_exp_f32_e32 v144, v101
	v_exp_f32_e32 v139, v102
	v_exp_f32_e32 v142, v103
	v_mfma_f32_32x32x16_bf16 v[50:65], v[180:183], v[86:89], v[50:65]
	s_cmp_ge_u32 s13, s30
	s_cbranch_scc1 .Lgqa_b_noload
	s_cmp_lt_u32 s13, s31
	s_cselect_b32 s9, 0, s31
	s_cselect_b32 s35, s12, s29
	s_lshl_b32 s9, s9, 6
	s_sub_i32 s9, s35, s9
	v_add_u32_e32 v118, s9, v137
	v_ashrrev_i32_e32 v119, 31, v118
	v_lshlrev_b64 v[118:119], 8, v[118:119]
	v_lshl_add_u64 v[120:121], v[16:17], 0, v[118:119]
	v_lshl_add_u64 v[122:123], v[134:135], 0, v[118:119]
	global_load_dwordx4 v[118:121], v[120:121], off
	s_nop 0
	global_load_dwordx4 v[122:125], v[122:123], off
.Lgqa_b_ld_done:
	s_waitcnt lgkmcnt(0)
	v_mfma_f32_32x32x16_bf16 v[34:49], v[224:227], v[156:159], v[34:49]
	s_waitcnt vmcnt(2)
	v_add_u32_e32 v252, s11, v187
	ds_write_b128 v252, v[130:133]
	v_add_u32_e32 v252, s11, v214
	ds_write_b128 v252, v[126:129] offset:12288
	v_exp_f32_e32 v138, v104
	v_exp_f32_e32 v140, v105
	v_mfma_f32_32x32x16_bf16 v[34:49], v[228:231], v[160:163], v[34:49]
	v_exp_f32_e32 v151, v106
	v_exp_f32_e32 v153, v107
	v_exp_f32_e32 v149, v108
	v_mfma_f32_32x32x16_bf16 v[34:49], v[232:235], v[82:85], v[34:49]
	v_exp_f32_e32 v152, v109
	v_exp_f32_e32 v147, v110
	v_exp_f32_e32 v150, v111
	v_mfma_f32_32x32x16_bf16 v[34:49], v[236:239], v[86:89], v[34:49]
	v_exp_f32_e32 v146, v112
	v_exp_f32_e32 v148, v113
	v_add_f32_e32 v252, v154, v155
	v_add_f32_e32 v136, v136, v252
	v_add_f32_e32 v252, v164, v165
	v_add_f32_e32 v136, v136, v252
	s_mov_b32 s9, s11
	s_add_i32 s13, s13, 2
	v_add_u32_e32 v137, 0x80, v137
	s_cmp_lt_u32 s8, s0
	s_cbranch_scc0 .Lgqa_exit
	s_mov_b32 s35, s10
	s_mov_b32 s10, s1
	s_branch .LBB0_497
